# speedup vs baseline: 1.0961x; 1.0134x over previous
.LBB1_69:
	s_or_b64 exec, exec, s[2:3]
	v_or_b32_e32 v100, v126, v125
	v_add_u32_e32 v104, 16, v100
	v_or_b32_e32 v101, v100, v121
	v_add_u16_e32 v102, v104, v121
	v_lshlrev_b32_e32 v101, 1, v101
	v_lshrrev_b16_e32 v102, 1, v102
	v_and_b32_e32 v101, 0x7fc, v101
	v_lshlrev_b32_e32 v102, 2, v102
	s_waitcnt vmcnt(0)
	s_barrier
	global_load_dword v101, v101, s[48:49]
	v_lshrrev_b32_e32 v103, 2, v107
	global_load_dword v102, v102, s[48:49]
	v_bitop3_b32 v108, v126, v124, v125 bitop3:0x36
	v_and_or_b32 v105, v103, 12, v127
	v_lshlrev_b32_e32 v103, 1, v108
	v_add_u32_e32 v108, 32, v100
	v_add_u16_e32 v113, v108, v121
	v_lshrrev_b16_e32 v113, 1, v113
	v_lshlrev_b32_e32 v113, 2, v113
	global_load_dword v113, v113, s[48:49]
	v_add_u32_e32 v110, 0x60, v100
	v_add_u32_e32 v111, 0x70, v100
	s_movk_i32 s1, 0x180
	v_or_b32_e32 v112, 0x80, v100
	v_mul_lo_u32 v105, v105, s1
	v_xor_b32_e32 v104, v104, v124
	v_add_u16_e32 v114, v110, v121
	v_add_u16_e32 v115, v111, v121
	v_add_u16_e32 v112, v112, v121
	v_add3_u32 v116, 0, v103, v105
	v_lshlrev_b32_e32 v103, 1, v104
	v_lshrrev_b16_e32 v104, 1, v114
	v_lshrrev_b16_e32 v114, 1, v115
	v_lshrrev_b16_e32 v112, 1, v112
	v_add3_u32 v115, 0, v103, v105
	v_lshlrev_b32_e32 v103, 2, v104
	v_lshlrev_b32_e32 v104, 2, v114
	v_lshlrev_b32_e32 v112, 2, v112
	global_load_dword v114, v103, s[48:49]
	s_nop 0
	global_load_dword v104, v104, s[48:49]
	s_nop 0
	global_load_dword v103, v112, s[48:49]
	s_movk_i32 s0, 0x80
	v_cmp_gt_i32_e64 s[2:3], s1, v107
	s_waitcnt vmcnt(5)
	v_fma_mixlo_f16 v82, v82, v101, 0
	v_fma_mixlo_f16 v83, v83, v101, 0
	s_waitcnt vmcnt(4)
	v_fma_mixlo_f16 v70, v70, v102, 0
	v_fma_mixlo_f16 v66, v66, v102, 0
	v_fma_mixlo_f16 v84, v84, v101, 0
	v_fma_mixlo_f16 v85, v85, v101, 0
	v_fma_mixlo_f16 v86, v86, v101, 0
	v_fma_mixlo_f16 v87, v87, v101, 0
	v_fma_mixlo_f16 v88, v88, v101, 0
	v_fma_mixlo_f16 v89, v89, v101, 0
	v_fma_mixlo_f16 v90, v90, v101, 0
	v_fma_mixlo_f16 v91, v91, v101, 0
	v_fma_mixlo_f16 v92, v92, v101, 0
	v_fma_mixlo_f16 v93, v93, v101, 0
	v_fma_mixlo_f16 v94, v94, v101, 0
	v_fma_mixlo_f16 v95, v95, v101, 0
	v_fma_mixlo_f16 v96, v96, v101, 0
	v_fma_mixlo_f16 v97, v97, v101, 0
	ds_write_b16 v116, v82
	ds_write_b16 v116, v83 offset:384
	ds_write_b16 v116, v84 offset:768
	ds_write_b16 v116, v85 offset:1152
	ds_write_b16 v116, v86 offset:6144
	ds_write_b16 v116, v87 offset:6528
	ds_write_b16 v116, v88 offset:6912
	ds_write_b16 v116, v89 offset:7296
	ds_write_b16 v116, v90 offset:49152
	ds_write_b16 v116, v91 offset:49536
	ds_write_b16 v116, v92 offset:49920
	ds_write_b16 v116, v93 offset:50304
	ds_write_b16 v116, v94 offset:55296
	ds_write_b16 v116, v95 offset:55680
	ds_write_b16 v116, v96 offset:56064
	ds_write_b16 v116, v97 offset:56448
	v_fma_mixlo_f16 v71, v71, v102, 0
	v_fma_mixlo_f16 v72, v72, v102, 0
	v_fma_mixlo_f16 v73, v73, v102, 0
	v_fma_mixlo_f16 v67, v67, v102, 0
	v_fma_mixlo_f16 v68, v68, v102, 0
	ds_write_b16 v115, v70
	ds_write_b16 v115, v71 offset:384
	ds_write_b16 v115, v72 offset:768
	ds_write_b16 v115, v73 offset:1152
	ds_write_b16 v115, v66 offset:6144
	ds_write_b16 v115, v67 offset:6528
	ds_write_b16 v115, v68 offset:6912
	v_fma_mixlo_f16 v66, v69, v102, 0
	ds_write_b16 v115, v66 offset:7296
	v_fma_mixlo_f16 v66, v78, v102, 0
	ds_write_b16 v115, v66 offset:49152
	v_fma_mixlo_f16 v66, v79, v102, 0
	ds_write_b16 v115, v66 offset:49536
	v_fma_mixlo_f16 v66, v80, v102, 0
	ds_write_b16 v115, v66 offset:49920
	v_fma_mixlo_f16 v66, v81, v102, 0
	ds_write_b16 v115, v66 offset:50304
	v_fma_mixlo_f16 v66, v74, v102, 0
	ds_write_b16 v115, v66 offset:55296
	v_fma_mixlo_f16 v66, v75, v102, 0
	ds_write_b16 v115, v66 offset:55680
	v_fma_mixlo_f16 v66, v76, v102, 0
	ds_write_b16 v115, v66 offset:56064
	v_fma_mixlo_f16 v66, v77, v102, 0
	ds_write_b16 v115, v66 offset:56448
	v_xor_b32_e32 v66, v108, v124
	v_lshlrev_b32_e32 v66, 1, v66
	v_add3_u32 v66, 0, v66, v105
	s_waitcnt vmcnt(3)
	v_fma_mixlo_f16 v42, v42, v113, 0
	ds_write_b16 v66, v42 offset:6144
	v_fma_mixlo_f16 v42, v43, v113, 0
	ds_write_b16 v66, v42 offset:6528
	v_fma_mixlo_f16 v42, v44, v113, 0
	ds_write_b16 v66, v42 offset:6912
	v_fma_mixlo_f16 v42, v45, v113, 0
	ds_write_b16 v66, v42 offset:7296
	v_fma_mixlo_f16 v42, v62, v113, 0
	ds_write_b16 v66, v42 offset:49152
	v_fma_mixlo_f16 v42, v63, v113, 0
	ds_write_b16 v66, v42 offset:49536
	v_fma_mixlo_f16 v42, v64, v113, 0
	ds_write_b16 v66, v42 offset:49920
	v_fma_mixlo_f16 v42, v65, v113, 0
	ds_write_b16 v66, v42 offset:50304
	v_fma_mixlo_f16 v42, v58, v113, 0
	ds_write_b16 v66, v42 offset:55296
	v_fma_mixlo_f16 v42, v59, v113, 0
	ds_write_b16 v66, v42 offset:55680
	v_fma_mixlo_f16 v42, v60, v113, 0
	ds_write_b16 v66, v42 offset:56064
	v_fma_mixlo_f16 v42, v61, v113, 0
	ds_write_b16 v66, v42 offset:56448
	v_xor_b32_e32 v42, v110, v124
	v_lshlrev_b32_e32 v42, 1, v42
	v_add3_u32 v42, 0, v42, v105
	s_waitcnt vmcnt(2)
	v_fma_mixlo_f16 v34, v34, v114, 0
	ds_write_b16 v42, v34 offset:6144
	v_fma_mixlo_f16 v34, v35, v114, 0
	ds_write_b16 v42, v34 offset:6528
	v_fma_mixlo_f16 v34, v36, v114, 0
	ds_write_b16 v42, v34 offset:6912
	v_fma_mixlo_f16 v34, v37, v114, 0
	ds_write_b16 v42, v34 offset:7296
	v_fma_mixlo_f16 v34, v54, v114, 0
	ds_write_b16 v42, v34 offset:49152
	v_fma_mixlo_f16 v34, v55, v114, 0
	ds_write_b16 v42, v34 offset:49536
	v_fma_mixlo_f16 v34, v56, v114, 0
	ds_write_b16 v42, v34 offset:49920
	v_fma_mixlo_f16 v34, v57, v114, 0
	ds_write_b16 v42, v34 offset:50304
	v_fma_mixlo_f16 v34, v50, v114, 0
	ds_write_b16 v42, v34 offset:55296
	v_fma_mixlo_f16 v34, v51, v114, 0
	ds_write_b16 v42, v34 offset:55680
	v_fma_mixlo_f16 v34, v52, v114, 0
	ds_write_b16 v42, v34 offset:56064
	v_fma_mixlo_f16 v34, v53, v114, 0
	ds_write_b16 v42, v34 offset:56448
	v_xor_b32_e32 v34, v111, v124
	v_lshlrev_b32_e32 v34, 1, v34
	v_add3_u32 v34, 0, v34, v105
	s_waitcnt vmcnt(1)
	v_fma_mixlo_f16 v18, v18, v104, 0
	ds_write_b16 v34, v18 offset:6144
	v_fma_mixlo_f16 v18, v19, v104, 0
	ds_write_b16 v34, v18 offset:6528
	v_fma_mixlo_f16 v18, v20, v104, 0
	ds_write_b16 v34, v18 offset:6912
	v_fma_mixlo_f16 v18, v21, v104, 0
	ds_write_b16 v34, v18 offset:7296
	v_fma_mixlo_f16 v18, v30, v104, 0
	ds_write_b16 v34, v18 offset:49152
	v_fma_mixlo_f16 v18, v31, v104, 0
	ds_write_b16 v34, v18 offset:49536
	v_fma_mixlo_f16 v18, v32, v104, 0
	ds_write_b16 v34, v18 offset:49920
	v_fma_mixlo_f16 v18, v33, v104, 0
	ds_write_b16 v34, v18 offset:50304
	v_fma_mixlo_f16 v18, v26, v104, 0
	ds_write_b16 v34, v18 offset:55296
	v_fma_mixlo_f16 v18, v27, v104, 0
	ds_write_b16 v34, v18 offset:55680
	v_fma_mixlo_f16 v18, v28, v104, 0
	ds_write_b16 v34, v18 offset:56064
	v_fma_mixlo_f16 v18, v29, v104, 0
	ds_write_b16 v34, v18 offset:56448
	v_bitop3_b32 v18, v100, v124, s0 bitop3:0x36
	v_lshlrev_b32_e32 v18, 1, v18
	v_add3_u32 v18, 0, v18, v105
	s_waitcnt vmcnt(0)
	v_fma_mixlo_f16 v2, v2, v103, 0
	ds_write_b16 v18, v2 offset:6144
	v_fma_mixlo_f16 v2, v3, v103, 0
	ds_write_b16 v18, v2 offset:6528
	v_fma_mixlo_f16 v2, v4, v103, 0
	ds_write_b16 v18, v2 offset:6912
	v_fma_mixlo_f16 v2, v5, v103, 0
	ds_write_b16 v18, v2 offset:7296
	v_fma_mixlo_f16 v2, v14, v103, 0
	ds_write_b16 v18, v2 offset:49152
	v_fma_mixlo_f16 v2, v15, v103, 0
	ds_write_b16 v18, v2 offset:49536
	v_fma_mixlo_f16 v2, v16, v103, 0
	ds_write_b16 v18, v2 offset:49920
	v_fma_mixlo_f16 v2, v17, v103, 0
	ds_write_b16 v18, v2 offset:50304
	v_fma_mixlo_f16 v2, v10, v103, 0
	ds_write_b16 v18, v2 offset:55296
	v_fma_mixlo_f16 v2, v11, v103, 0
	ds_write_b16 v18, v2 offset:55680
	v_fma_mixlo_f16 v2, v12, v103, 0
	v_fma_mixlo_f16 v46, v46, v113, 0
	ds_write_b16 v18, v2 offset:56064
	v_fma_mixlo_f16 v2, v13, v103, 0
	s_mov_b32 s0, 0x2aaaaaab
	ds_write_b16 v66, v46
	v_fma_mixlo_f16 v46, v47, v113, 0
	ds_write_b16 v18, v2 offset:56448
	v_mul_hi_i32 v2, v107, s0
	ds_write_b16 v66, v46 offset:384
	v_fma_mixlo_f16 v46, v48, v113, 0
	v_fma_mixlo_f16 v38, v38, v114, 0
	v_lshrrev_b32_e32 v3, 31, v2
	v_ashrrev_i32_e32 v2, 4, v2
	ds_write_b16 v66, v46 offset:768
	v_fma_mixlo_f16 v46, v49, v113, 0
	ds_write_b16 v42, v38
	v_fma_mixlo_f16 v38, v39, v114, 0
	v_fma_mixlo_f16 v22, v22, v104, 0
	v_fma_mixlo_f16 v6, v6, v103, 0
	v_add_u32_e32 v49, v2, v3
	s_movk_i32 s0, 0x60
	ds_write_b16 v42, v38 offset:384
	v_fma_mixlo_f16 v38, v40, v114, 0
	ds_write_b16 v34, v22
	v_fma_mixlo_f16 v22, v23, v104, 0
	ds_write_b16 v18, v6
	v_fma_mixlo_f16 v6, v7, v103, 0
	v_mul_lo_u32 v2, v49, s0
	ds_write_b16 v66, v46 offset:1152
	ds_write_b16 v42, v38 offset:768
	v_fma_mixlo_f16 v38, v41, v114, 0
	ds_write_b16 v34, v22 offset:384
	v_fma_mixlo_f16 v22, v24, v104, 0
	ds_write_b16 v18, v6 offset:384
	v_fma_mixlo_f16 v6, v8, v103, 0
	v_sub_u32_e32 v14, v107, v2
	v_lshrrev_b32_e32 v2, 1, v121
	s_movk_i32 s0, 0x5e80
	ds_write_b16 v42, v38 offset:1152
	ds_write_b16 v34, v22 offset:768
	v_fma_mixlo_f16 v22, v25, v104, 0
	ds_write_b16 v18, v6 offset:768
	v_fma_mixlo_f16 v6, v9, v103, 0
	v_add_u32_e32 v8, v14, v2
	v_mov_b32_e32 v7, 0
	v_lshlrev_b32_e32 v2, 2, v14
	v_mul_lo_u32 v3, v49, s0
	ds_write_b16 v34, v22 offset:1152
	ds_write_b16 v18, v6 offset:1152
	v_ashrrev_i32_e32 v9, 31, v8
	v_mul_lo_u32 v45, v49, s75
	v_xor_b32_e32 v48, 0x60, v2
	v_xor_b32_e32 v47, 64, v2
	v_xor_b32_e32 v46, 32, v2
	v_add3_u32 v44, v3, v123, 0
	v_mov_b32_e32 v6, v7
	v_mov_b32_e32 v3, v7
	v_mov_b32_e32 v4, v7
	s_waitcnt lgkmcnt(0)
	s_barrier
	s_and_saveexec_b64 s[0:1], s[2:3]
	s_cbranch_execz .LBB1_73
	v_readlane_b32 s4, v230, 2
	v_readlane_b32 s5, v230, 3
	v_mov_b32_e32 v12, 0
	v_mov_b32_e32 v13, v12
	v_lshl_add_u64 v[4:5], v[8:9], 3, s[4:5]
	global_load_dwordx2 v[2:3], v[4:5], off
	global_load_dwordx2 v[6:7], v[4:5], off offset:3072
	v_readlane_b32 s4, v230, 10
	v_readlane_b32 s6, v230, 4
	v_readlane_b32 s7, v230, 5
	v_add3_u32 v15, v45, v48, s4
	s_add_i32 s4, 0, 0xc00
	v_add3_u32 v16, v45, v47, s4
	s_add_i32 s4, 0, 0x600
	v_add3_u32 v17, v45, v46, s4
	v_mov_b32_e32 v26, v44
	v_add_u32_e32 v27, 0x200, v44
	v_mov_b32_e32 v28, v17
	v_add_u32_e32 v29, 0x200, v17
	v_mov_b32_e32 v30, v16
	v_add_u32_e32 v31, 0x200, v16
	v_mov_b32_e32 v32, v15
	v_add_u32_e32 v33, 0x200, v15
	ds_read2_b32 v[50:51], v26 offset1:96
	ds_read2_b32 v[52:53], v27 offset0:64 offset1:160
	ds_read2_b32 v[54:55], v28 offset1:96
	ds_read2_b32 v[56:57], v29 offset0:64 offset1:160
	v_add_u32_e32 v26, 0x1800, v26
	v_add_u32_e32 v27, 0x1800, v27
	v_add_u32_e32 v28, 0x1800, v28
	v_add_u32_e32 v29, 0x1800, v29
	ds_read2_b32 v[58:59], v30 offset1:96
	ds_read2_b32 v[60:61], v31 offset0:64 offset1:160
	ds_read2_b32 v[62:63], v32 offset1:96
	ds_read2_b32 v[64:65], v33 offset0:64 offset1:160
	v_add_u32_e32 v30, 0x1800, v30
	v_add_u32_e32 v31, 0x1800, v31
	v_add_u32_e32 v32, 0x1800, v32
	v_add_u32_e32 v33, 0x1800, v33
	ds_read2_b32 v[66:67], v26 offset1:96
	ds_read2_b32 v[68:69], v27 offset0:64 offset1:160
	ds_read2_b32 v[70:71], v28 offset1:96
	ds_read2_b32 v[72:73], v29 offset0:64 offset1:160
	v_add_u32_e32 v26, 0x1800, v26
	v_add_u32_e32 v27, 0x1800, v27
	v_add_u32_e32 v28, 0x1800, v28
	v_add_u32_e32 v29, 0x1800, v29
	s_waitcnt vmcnt(1)
	v_xor_b32_e32 v4, 0x80000000, v3
	v_mov_b32_e32 v10, v2
	v_mov_b32_e32 v11, v2
	v_mov_b32_e32 v5, v3
	s_waitcnt lgkmcnt(8)
	v_cvt_f32_f16_e32 v74, v50
	v_cvt_f32_f16_sdwa v75, v50 dst_sel:DWORD dst_unused:UNUSED_PAD src0_sel:WORD_1
	v_cvt_f32_f16_e32 v76, v51
	v_cvt_f32_f16_sdwa v77, v51 dst_sel:DWORD dst_unused:UNUSED_PAD src0_sel:WORD_1
	v_cvt_f32_f16_e32 v78, v52
	v_cvt_f32_f16_sdwa v79, v52 dst_sel:DWORD dst_unused:UNUSED_PAD src0_sel:WORD_1
	v_cvt_f32_f16_e32 v80, v53
	v_cvt_f32_f16_sdwa v81, v53 dst_sel:DWORD dst_unused:UNUSED_PAD src0_sel:WORD_1
	v_cvt_f32_f16_e32 v82, v54
	v_cvt_f32_f16_sdwa v83, v54 dst_sel:DWORD dst_unused:UNUSED_PAD src0_sel:WORD_1
	v_cvt_f32_f16_e32 v84, v55
	v_cvt_f32_f16_sdwa v85, v55 dst_sel:DWORD dst_unused:UNUSED_PAD src0_sel:WORD_1
	v_cvt_f32_f16_e32 v86, v56
	v_cvt_f32_f16_sdwa v87, v56 dst_sel:DWORD dst_unused:UNUSED_PAD src0_sel:WORD_1
	v_cvt_f32_f16_e32 v88, v57
	v_cvt_f32_f16_sdwa v89, v57 dst_sel:DWORD dst_unused:UNUSED_PAD src0_sel:WORD_1
	ds_read2_b32 v[50:51], v30 offset1:96
	ds_read2_b32 v[52:53], v31 offset0:64 offset1:160
	ds_read2_b32 v[54:55], v32 offset1:96
	ds_read2_b32 v[56:57], v33 offset0:64 offset1:160
	v_add_u32_e32 v30, 0x1800, v30
	v_add_u32_e32 v31, 0x1800, v31
	v_add_u32_e32 v32, 0x1800, v32
	v_add_u32_e32 v33, 0x1800, v33
	s_waitcnt lgkmcnt(8)
	v_pk_fma_f32 v[74:75], v[4:5], v[12:13], v[74:75] op_sel:[0,1,0] op_sel_hi:[1,0,1]
	v_cvt_f32_f16_e32 v90, v58
	v_pk_fma_f32 v[12:13], v[10:11], v[12:13], v[74:75]
	v_cvt_f32_f16_sdwa v91, v58 dst_sel:DWORD dst_unused:UNUSED_PAD src0_sel:WORD_1
	v_pk_fma_f32 v[76:77], v[4:5], v[12:13], v[76:77] op_sel:[0,1,0] op_sel_hi:[1,0,1]
	v_cvt_f32_f16_e32 v92, v59
	v_pk_fma_f32 v[12:13], v[10:11], v[12:13], v[76:77]
	v_cvt_f32_f16_sdwa v93, v59 dst_sel:DWORD dst_unused:UNUSED_PAD src0_sel:WORD_1
	v_pk_fma_f32 v[78:79], v[4:5], v[12:13], v[78:79] op_sel:[0,1,0] op_sel_hi:[1,0,1]
	v_cvt_f32_f16_e32 v94, v60
	v_pk_fma_f32 v[12:13], v[10:11], v[12:13], v[78:79]
	v_cvt_f32_f16_sdwa v95, v60 dst_sel:DWORD dst_unused:UNUSED_PAD src0_sel:WORD_1
	v_pk_fma_f32 v[80:81], v[4:5], v[12:13], v[80:81] op_sel:[0,1,0] op_sel_hi:[1,0,1]
	v_cvt_f32_f16_e32 v96, v61
	v_pk_fma_f32 v[12:13], v[10:11], v[12:13], v[80:81]
	v_cvt_f32_f16_sdwa v97, v61 dst_sel:DWORD dst_unused:UNUSED_PAD src0_sel:WORD_1
	v_pk_fma_f32 v[82:83], v[4:5], v[12:13], v[82:83] op_sel:[0,1,0] op_sel_hi:[1,0,1]
	v_cvt_f32_f16_e32 v18, v62
	v_pk_fma_f32 v[12:13], v[10:11], v[12:13], v[82:83]
	v_cvt_f32_f16_sdwa v19, v62 dst_sel:DWORD dst_unused:UNUSED_PAD src0_sel:WORD_1
	v_pk_fma_f32 v[84:85], v[4:5], v[12:13], v[84:85] op_sel:[0,1,0] op_sel_hi:[1,0,1]
	v_cvt_f32_f16_e32 v20, v63
	v_pk_fma_f32 v[12:13], v[10:11], v[12:13], v[84:85]
	v_cvt_f32_f16_sdwa v21, v63 dst_sel:DWORD dst_unused:UNUSED_PAD src0_sel:WORD_1
	v_pk_fma_f32 v[86:87], v[4:5], v[12:13], v[86:87] op_sel:[0,1,0] op_sel_hi:[1,0,1]
	v_cvt_f32_f16_e32 v22, v64
	v_pk_fma_f32 v[12:13], v[10:11], v[12:13], v[86:87]
	v_cvt_f32_f16_sdwa v23, v64 dst_sel:DWORD dst_unused:UNUSED_PAD src0_sel:WORD_1
	v_pk_fma_f32 v[88:89], v[4:5], v[12:13], v[88:89] op_sel:[0,1,0] op_sel_hi:[1,0,1]
	v_cvt_f32_f16_e32 v24, v65
	v_pk_fma_f32 v[12:13], v[10:11], v[12:13], v[88:89]
	v_cvt_f32_f16_sdwa v25, v65 dst_sel:DWORD dst_unused:UNUSED_PAD src0_sel:WORD_1
	ds_read2_b32 v[58:59], v26 offset1:96
	ds_read2_b32 v[60:61], v27 offset0:64 offset1:160
	ds_read2_b32 v[62:63], v28 offset1:96
	ds_read2_b32 v[64:65], v29 offset0:64 offset1:160
	v_add_u32_e32 v26, 0x1800, v26
	v_add_u32_e32 v27, 0x1800, v27
	v_add_u32_e32 v28, 0x1800, v28
	v_add_u32_e32 v29, 0x1800, v29
	s_waitcnt lgkmcnt(8)
	v_pk_fma_f32 v[90:91], v[4:5], v[12:13], v[90:91] op_sel:[0,1,0] op_sel_hi:[1,0,1]
	v_cvt_f32_f16_e32 v74, v66
	v_pk_fma_f32 v[12:13], v[10:11], v[12:13], v[90:91]
	v_cvt_f32_f16_sdwa v75, v66 dst_sel:DWORD dst_unused:UNUSED_PAD src0_sel:WORD_1
	v_pk_fma_f32 v[92:93], v[4:5], v[12:13], v[92:93] op_sel:[0,1,0] op_sel_hi:[1,0,1]
	v_cvt_f32_f16_e32 v76, v67
	v_pk_fma_f32 v[12:13], v[10:11], v[12:13], v[92:93]
	v_cvt_f32_f16_sdwa v77, v67 dst_sel:DWORD dst_unused:UNUSED_PAD src0_sel:WORD_1
	v_pk_fma_f32 v[94:95], v[4:5], v[12:13], v[94:95] op_sel:[0,1,0] op_sel_hi:[1,0,1]
	v_cvt_f32_f16_e32 v78, v68
	v_pk_fma_f32 v[12:13], v[10:11], v[12:13], v[94:95]
	v_cvt_f32_f16_sdwa v79, v68 dst_sel:DWORD dst_unused:UNUSED_PAD src0_sel:WORD_1
	v_pk_fma_f32 v[96:97], v[4:5], v[12:13], v[96:97] op_sel:[0,1,0] op_sel_hi:[1,0,1]
	v_cvt_f32_f16_e32 v80, v69
	v_pk_fma_f32 v[12:13], v[10:11], v[12:13], v[96:97]
	v_cvt_f32_f16_sdwa v81, v69 dst_sel:DWORD dst_unused:UNUSED_PAD src0_sel:WORD_1
	v_pk_fma_f32 v[18:19], v[4:5], v[12:13], v[18:19] op_sel:[0,1,0] op_sel_hi:[1,0,1]
	v_cvt_f32_f16_e32 v82, v70
	v_pk_fma_f32 v[12:13], v[10:11], v[12:13], v[18:19]
	v_cvt_f32_f16_sdwa v83, v70 dst_sel:DWORD dst_unused:UNUSED_PAD src0_sel:WORD_1
	v_pk_fma_f32 v[20:21], v[4:5], v[12:13], v[20:21] op_sel:[0,1,0] op_sel_hi:[1,0,1]
	v_cvt_f32_f16_e32 v84, v71
	v_pk_fma_f32 v[12:13], v[10:11], v[12:13], v[20:21]
	v_cvt_f32_f16_sdwa v85, v71 dst_sel:DWORD dst_unused:UNUSED_PAD src0_sel:WORD_1
	v_pk_fma_f32 v[22:23], v[4:5], v[12:13], v[22:23] op_sel:[0,1,0] op_sel_hi:[1,0,1]
	v_cvt_f32_f16_e32 v86, v72
	v_pk_fma_f32 v[12:13], v[10:11], v[12:13], v[22:23]
	v_cvt_f32_f16_sdwa v87, v72 dst_sel:DWORD dst_unused:UNUSED_PAD src0_sel:WORD_1
	v_pk_fma_f32 v[24:25], v[4:5], v[12:13], v[24:25] op_sel:[0,1,0] op_sel_hi:[1,0,1]
	v_cvt_f32_f16_e32 v88, v73
	v_pk_fma_f32 v[12:13], v[10:11], v[12:13], v[24:25]
	v_cvt_f32_f16_sdwa v89, v73 dst_sel:DWORD dst_unused:UNUSED_PAD src0_sel:WORD_1
	ds_read2_b32 v[66:67], v30 offset1:96
	ds_read2_b32 v[68:69], v31 offset0:64 offset1:160
	ds_read2_b32 v[70:71], v32 offset1:96
	ds_read2_b32 v[72:73], v33 offset0:64 offset1:160
	v_add_u32_e32 v30, 0x1800, v30
	v_add_u32_e32 v31, 0x1800, v31
	v_add_u32_e32 v32, 0x1800, v32
	v_add_u32_e32 v33, 0x1800, v33
	s_waitcnt lgkmcnt(8)
	v_pk_fma_f32 v[74:75], v[4:5], v[12:13], v[74:75] op_sel:[0,1,0] op_sel_hi:[1,0,1]
	v_cvt_f32_f16_e32 v90, v50
	v_pk_fma_f32 v[12:13], v[10:11], v[12:13], v[74:75]
	v_cvt_f32_f16_sdwa v91, v50 dst_sel:DWORD dst_unused:UNUSED_PAD src0_sel:WORD_1
	v_pk_fma_f32 v[76:77], v[4:5], v[12:13], v[76:77] op_sel:[0,1,0] op_sel_hi:[1,0,1]
	v_cvt_f32_f16_e32 v92, v51
	v_pk_fma_f32 v[12:13], v[10:11], v[12:13], v[76:77]
	v_cvt_f32_f16_sdwa v93, v51 dst_sel:DWORD dst_unused:UNUSED_PAD src0_sel:WORD_1
	v_pk_fma_f32 v[78:79], v[4:5], v[12:13], v[78:79] op_sel:[0,1,0] op_sel_hi:[1,0,1]
	v_cvt_f32_f16_e32 v94, v52
	v_pk_fma_f32 v[12:13], v[10:11], v[12:13], v[78:79]
	v_cvt_f32_f16_sdwa v95, v52 dst_sel:DWORD dst_unused:UNUSED_PAD src0_sel:WORD_1
	v_pk_fma_f32 v[80:81], v[4:5], v[12:13], v[80:81] op_sel:[0,1,0] op_sel_hi:[1,0,1]
	v_cvt_f32_f16_e32 v96, v53
	v_pk_fma_f32 v[12:13], v[10:11], v[12:13], v[80:81]
	v_cvt_f32_f16_sdwa v97, v53 dst_sel:DWORD dst_unused:UNUSED_PAD src0_sel:WORD_1
	v_pk_fma_f32 v[82:83], v[4:5], v[12:13], v[82:83] op_sel:[0,1,0] op_sel_hi:[1,0,1]
	v_cvt_f32_f16_e32 v18, v54
	v_pk_fma_f32 v[12:13], v[10:11], v[12:13], v[82:83]
	v_cvt_f32_f16_sdwa v19, v54 dst_sel:DWORD dst_unused:UNUSED_PAD src0_sel:WORD_1
	v_pk_fma_f32 v[84:85], v[4:5], v[12:13], v[84:85] op_sel:[0,1,0] op_sel_hi:[1,0,1]
	v_cvt_f32_f16_e32 v20, v55
	v_pk_fma_f32 v[12:13], v[10:11], v[12:13], v[84:85]
	v_cvt_f32_f16_sdwa v21, v55 dst_sel:DWORD dst_unused:UNUSED_PAD src0_sel:WORD_1
	v_pk_fma_f32 v[86:87], v[4:5], v[12:13], v[86:87] op_sel:[0,1,0] op_sel_hi:[1,0,1]
	v_cvt_f32_f16_e32 v22, v56
	v_pk_fma_f32 v[12:13], v[10:11], v[12:13], v[86:87]
	v_cvt_f32_f16_sdwa v23, v56 dst_sel:DWORD dst_unused:UNUSED_PAD src0_sel:WORD_1
	v_pk_fma_f32 v[88:89], v[4:5], v[12:13], v[88:89] op_sel:[0,1,0] op_sel_hi:[1,0,1]
	v_cvt_f32_f16_e32 v24, v57
	v_pk_fma_f32 v[12:13], v[10:11], v[12:13], v[88:89]
	v_cvt_f32_f16_sdwa v25, v57 dst_sel:DWORD dst_unused:UNUSED_PAD src0_sel:WORD_1
	ds_read2_b32 v[50:51], v26 offset1:96
	ds_read2_b32 v[52:53], v27 offset0:64 offset1:160
	ds_read2_b32 v[54:55], v28 offset1:96
	ds_read2_b32 v[56:57], v29 offset0:64 offset1:160
	v_add_u32_e32 v26, 0x1800, v26
	v_add_u32_e32 v27, 0x1800, v27
	v_add_u32_e32 v28, 0x1800, v28
	v_add_u32_e32 v29, 0x1800, v29
	s_waitcnt lgkmcnt(8)
	v_pk_fma_f32 v[90:91], v[4:5], v[12:13], v[90:91] op_sel:[0,1,0] op_sel_hi:[1,0,1]
	v_cvt_f32_f16_e32 v74, v58
	v_pk_fma_f32 v[12:13], v[10:11], v[12:13], v[90:91]
	v_cvt_f32_f16_sdwa v75, v58 dst_sel:DWORD dst_unused:UNUSED_PAD src0_sel:WORD_1
	v_pk_fma_f32 v[92:93], v[4:5], v[12:13], v[92:93] op_sel:[0,1,0] op_sel_hi:[1,0,1]
	v_cvt_f32_f16_e32 v76, v59
	v_pk_fma_f32 v[12:13], v[10:11], v[12:13], v[92:93]
	v_cvt_f32_f16_sdwa v77, v59 dst_sel:DWORD dst_unused:UNUSED_PAD src0_sel:WORD_1
	v_pk_fma_f32 v[94:95], v[4:5], v[12:13], v[94:95] op_sel:[0,1,0] op_sel_hi:[1,0,1]
	v_cvt_f32_f16_e32 v78, v60
	v_pk_fma_f32 v[12:13], v[10:11], v[12:13], v[94:95]
	v_cvt_f32_f16_sdwa v79, v60 dst_sel:DWORD dst_unused:UNUSED_PAD src0_sel:WORD_1
	v_pk_fma_f32 v[96:97], v[4:5], v[12:13], v[96:97] op_sel:[0,1,0] op_sel_hi:[1,0,1]
	v_cvt_f32_f16_e32 v80, v61
	v_pk_fma_f32 v[12:13], v[10:11], v[12:13], v[96:97]
	v_cvt_f32_f16_sdwa v81, v61 dst_sel:DWORD dst_unused:UNUSED_PAD src0_sel:WORD_1
	v_pk_fma_f32 v[18:19], v[4:5], v[12:13], v[18:19] op_sel:[0,1,0] op_sel_hi:[1,0,1]
	v_cvt_f32_f16_e32 v82, v62
	v_pk_fma_f32 v[12:13], v[10:11], v[12:13], v[18:19]
	v_cvt_f32_f16_sdwa v83, v62 dst_sel:DWORD dst_unused:UNUSED_PAD src0_sel:WORD_1
	v_pk_fma_f32 v[20:21], v[4:5], v[12:13], v[20:21] op_sel:[0,1,0] op_sel_hi:[1,0,1]
	v_cvt_f32_f16_e32 v84, v63
	v_pk_fma_f32 v[12:13], v[10:11], v[12:13], v[20:21]
	v_cvt_f32_f16_sdwa v85, v63 dst_sel:DWORD dst_unused:UNUSED_PAD src0_sel:WORD_1
	v_pk_fma_f32 v[22:23], v[4:5], v[12:13], v[22:23] op_sel:[0,1,0] op_sel_hi:[1,0,1]
	v_cvt_f32_f16_e32 v86, v64
	v_pk_fma_f32 v[12:13], v[10:11], v[12:13], v[22:23]
	v_cvt_f32_f16_sdwa v87, v64 dst_sel:DWORD dst_unused:UNUSED_PAD src0_sel:WORD_1
	v_pk_fma_f32 v[24:25], v[4:5], v[12:13], v[24:25] op_sel:[0,1,0] op_sel_hi:[1,0,1]
	v_cvt_f32_f16_e32 v88, v65
	v_pk_fma_f32 v[12:13], v[10:11], v[12:13], v[24:25]
	v_cvt_f32_f16_sdwa v89, v65 dst_sel:DWORD dst_unused:UNUSED_PAD src0_sel:WORD_1
	ds_read2_b32 v[58:59], v30 offset1:96
	ds_read2_b32 v[60:61], v31 offset0:64 offset1:160
	ds_read2_b32 v[62:63], v32 offset1:96
	ds_read2_b32 v[64:65], v33 offset0:64 offset1:160
	v_add_u32_e32 v30, 0x1800, v30
	v_add_u32_e32 v31, 0x1800, v31
	v_add_u32_e32 v32, 0x1800, v32
	v_add_u32_e32 v33, 0x1800, v33
	s_waitcnt lgkmcnt(8)
	v_pk_fma_f32 v[74:75], v[4:5], v[12:13], v[74:75] op_sel:[0,1,0] op_sel_hi:[1,0,1]
	v_cvt_f32_f16_e32 v90, v66
	v_pk_fma_f32 v[12:13], v[10:11], v[12:13], v[74:75]
	v_cvt_f32_f16_sdwa v91, v66 dst_sel:DWORD dst_unused:UNUSED_PAD src0_sel:WORD_1
	v_pk_fma_f32 v[76:77], v[4:5], v[12:13], v[76:77] op_sel:[0,1,0] op_sel_hi:[1,0,1]
	v_cvt_f32_f16_e32 v92, v67
	v_pk_fma_f32 v[12:13], v[10:11], v[12:13], v[76:77]
	v_cvt_f32_f16_sdwa v93, v67 dst_sel:DWORD dst_unused:UNUSED_PAD src0_sel:WORD_1
	v_pk_fma_f32 v[78:79], v[4:5], v[12:13], v[78:79] op_sel:[0,1,0] op_sel_hi:[1,0,1]
	v_cvt_f32_f16_e32 v94, v68
	v_pk_fma_f32 v[12:13], v[10:11], v[12:13], v[78:79]
	v_cvt_f32_f16_sdwa v95, v68 dst_sel:DWORD dst_unused:UNUSED_PAD src0_sel:WORD_1
	v_pk_fma_f32 v[80:81], v[4:5], v[12:13], v[80:81] op_sel:[0,1,0] op_sel_hi:[1,0,1]
	v_cvt_f32_f16_e32 v96, v69
	v_pk_fma_f32 v[12:13], v[10:11], v[12:13], v[80:81]
	v_cvt_f32_f16_sdwa v97, v69 dst_sel:DWORD dst_unused:UNUSED_PAD src0_sel:WORD_1
	v_pk_fma_f32 v[82:83], v[4:5], v[12:13], v[82:83] op_sel:[0,1,0] op_sel_hi:[1,0,1]
	v_cvt_f32_f16_e32 v18, v70
	v_pk_fma_f32 v[12:13], v[10:11], v[12:13], v[82:83]
	v_cvt_f32_f16_sdwa v19, v70 dst_sel:DWORD dst_unused:UNUSED_PAD src0_sel:WORD_1
	v_pk_fma_f32 v[84:85], v[4:5], v[12:13], v[84:85] op_sel:[0,1,0] op_sel_hi:[1,0,1]
	v_cvt_f32_f16_e32 v20, v71
	v_pk_fma_f32 v[12:13], v[10:11], v[12:13], v[84:85]
	v_cvt_f32_f16_sdwa v21, v71 dst_sel:DWORD dst_unused:UNUSED_PAD src0_sel:WORD_1
	v_pk_fma_f32 v[86:87], v[4:5], v[12:13], v[86:87] op_sel:[0,1,0] op_sel_hi:[1,0,1]
	v_cvt_f32_f16_e32 v22, v72
	v_pk_fma_f32 v[12:13], v[10:11], v[12:13], v[86:87]
	v_cvt_f32_f16_sdwa v23, v72 dst_sel:DWORD dst_unused:UNUSED_PAD src0_sel:WORD_1
	v_pk_fma_f32 v[88:89], v[4:5], v[12:13], v[88:89] op_sel:[0,1,0] op_sel_hi:[1,0,1]
	v_cvt_f32_f16_e32 v24, v73
	v_pk_fma_f32 v[12:13], v[10:11], v[12:13], v[88:89]
	v_cvt_f32_f16_sdwa v25, v73 dst_sel:DWORD dst_unused:UNUSED_PAD src0_sel:WORD_1
	s_waitcnt lgkmcnt(4)
	v_pk_fma_f32 v[90:91], v[4:5], v[12:13], v[90:91] op_sel:[0,1,0] op_sel_hi:[1,0,1]
	v_cvt_f32_f16_e32 v74, v50
	v_pk_fma_f32 v[12:13], v[10:11], v[12:13], v[90:91]
	v_cvt_f32_f16_sdwa v75, v50 dst_sel:DWORD dst_unused:UNUSED_PAD src0_sel:WORD_1
	v_pk_fma_f32 v[92:93], v[4:5], v[12:13], v[92:93] op_sel:[0,1,0] op_sel_hi:[1,0,1]
	v_cvt_f32_f16_e32 v76, v51
	v_pk_fma_f32 v[12:13], v[10:11], v[12:13], v[92:93]
	v_cvt_f32_f16_sdwa v77, v51 dst_sel:DWORD dst_unused:UNUSED_PAD src0_sel:WORD_1
	v_pk_fma_f32 v[94:95], v[4:5], v[12:13], v[94:95] op_sel:[0,1,0] op_sel_hi:[1,0,1]
	v_cvt_f32_f16_e32 v78, v52
	v_pk_fma_f32 v[12:13], v[10:11], v[12:13], v[94:95]
	v_cvt_f32_f16_sdwa v79, v52 dst_sel:DWORD dst_unused:UNUSED_PAD src0_sel:WORD_1
	v_pk_fma_f32 v[96:97], v[4:5], v[12:13], v[96:97] op_sel:[0,1,0] op_sel_hi:[1,0,1]
	v_cvt_f32_f16_e32 v80, v53
	v_pk_fma_f32 v[12:13], v[10:11], v[12:13], v[96:97]
	v_cvt_f32_f16_sdwa v81, v53 dst_sel:DWORD dst_unused:UNUSED_PAD src0_sel:WORD_1
	v_pk_fma_f32 v[18:19], v[4:5], v[12:13], v[18:19] op_sel:[0,1,0] op_sel_hi:[1,0,1]
	v_cvt_f32_f16_e32 v82, v54
	v_pk_fma_f32 v[12:13], v[10:11], v[12:13], v[18:19]
	v_cvt_f32_f16_sdwa v83, v54 dst_sel:DWORD dst_unused:UNUSED_PAD src0_sel:WORD_1
	v_pk_fma_f32 v[20:21], v[4:5], v[12:13], v[20:21] op_sel:[0,1,0] op_sel_hi:[1,0,1]
	v_cvt_f32_f16_e32 v84, v55
	v_pk_fma_f32 v[12:13], v[10:11], v[12:13], v[20:21]
	v_cvt_f32_f16_sdwa v85, v55 dst_sel:DWORD dst_unused:UNUSED_PAD src0_sel:WORD_1
	v_pk_fma_f32 v[22:23], v[4:5], v[12:13], v[22:23] op_sel:[0,1,0] op_sel_hi:[1,0,1]
	v_cvt_f32_f16_e32 v86, v56
	v_pk_fma_f32 v[12:13], v[10:11], v[12:13], v[22:23]
	v_cvt_f32_f16_sdwa v87, v56 dst_sel:DWORD dst_unused:UNUSED_PAD src0_sel:WORD_1
	v_pk_fma_f32 v[24:25], v[4:5], v[12:13], v[24:25] op_sel:[0,1,0] op_sel_hi:[1,0,1]
	v_cvt_f32_f16_e32 v88, v57
	v_pk_fma_f32 v[12:13], v[10:11], v[12:13], v[24:25]
	v_cvt_f32_f16_sdwa v89, v57 dst_sel:DWORD dst_unused:UNUSED_PAD src0_sel:WORD_1
	s_waitcnt lgkmcnt(0)
	v_pk_fma_f32 v[74:75], v[4:5], v[12:13], v[74:75] op_sel:[0,1,0] op_sel_hi:[1,0,1]
	v_cvt_f32_f16_e32 v90, v58
	v_pk_fma_f32 v[12:13], v[10:11], v[12:13], v[74:75]
	v_cvt_f32_f16_sdwa v91, v58 dst_sel:DWORD dst_unused:UNUSED_PAD src0_sel:WORD_1
	v_pk_fma_f32 v[76:77], v[4:5], v[12:13], v[76:77] op_sel:[0,1,0] op_sel_hi:[1,0,1]
	v_cvt_f32_f16_e32 v92, v59
	v_pk_fma_f32 v[12:13], v[10:11], v[12:13], v[76:77]
	v_cvt_f32_f16_sdwa v93, v59 dst_sel:DWORD dst_unused:UNUSED_PAD src0_sel:WORD_1
	v_pk_fma_f32 v[78:79], v[4:5], v[12:13], v[78:79] op_sel:[0,1,0] op_sel_hi:[1,0,1]
	v_cvt_f32_f16_e32 v94, v60
	v_pk_fma_f32 v[12:13], v[10:11], v[12:13], v[78:79]
	v_cvt_f32_f16_sdwa v95, v60 dst_sel:DWORD dst_unused:UNUSED_PAD src0_sel:WORD_1
	v_pk_fma_f32 v[80:81], v[4:5], v[12:13], v[80:81] op_sel:[0,1,0] op_sel_hi:[1,0,1]
	v_cvt_f32_f16_e32 v96, v61
	v_pk_fma_f32 v[12:13], v[10:11], v[12:13], v[80:81]
	v_cvt_f32_f16_sdwa v97, v61 dst_sel:DWORD dst_unused:UNUSED_PAD src0_sel:WORD_1
	v_pk_fma_f32 v[82:83], v[4:5], v[12:13], v[82:83] op_sel:[0,1,0] op_sel_hi:[1,0,1]
	v_cvt_f32_f16_e32 v18, v62
	v_pk_fma_f32 v[12:13], v[10:11], v[12:13], v[82:83]
	v_cvt_f32_f16_sdwa v19, v62 dst_sel:DWORD dst_unused:UNUSED_PAD src0_sel:WORD_1
	v_pk_fma_f32 v[84:85], v[4:5], v[12:13], v[84:85] op_sel:[0,1,0] op_sel_hi:[1,0,1]
	v_cvt_f32_f16_e32 v20, v63
	v_pk_fma_f32 v[12:13], v[10:11], v[12:13], v[84:85]
	v_cvt_f32_f16_sdwa v21, v63 dst_sel:DWORD dst_unused:UNUSED_PAD src0_sel:WORD_1
	v_pk_fma_f32 v[86:87], v[4:5], v[12:13], v[86:87] op_sel:[0,1,0] op_sel_hi:[1,0,1]
	v_cvt_f32_f16_e32 v22, v64
	v_pk_fma_f32 v[12:13], v[10:11], v[12:13], v[86:87]
	v_cvt_f32_f16_sdwa v23, v64 dst_sel:DWORD dst_unused:UNUSED_PAD src0_sel:WORD_1
	v_pk_fma_f32 v[88:89], v[4:5], v[12:13], v[88:89] op_sel:[0,1,0] op_sel_hi:[1,0,1]
	v_cvt_f32_f16_e32 v24, v65
	v_pk_fma_f32 v[12:13], v[10:11], v[12:13], v[88:89]
	v_cvt_f32_f16_sdwa v25, v65 dst_sel:DWORD dst_unused:UNUSED_PAD src0_sel:WORD_1
	v_pk_fma_f32 v[90:91], v[4:5], v[12:13], v[90:91] op_sel:[0,1,0] op_sel_hi:[1,0,1]
	s_nop 0
	v_pk_fma_f32 v[12:13], v[10:11], v[12:13], v[90:91]
	s_nop 0
	v_pk_fma_f32 v[92:93], v[4:5], v[12:13], v[92:93] op_sel:[0,1,0] op_sel_hi:[1,0,1]
	s_nop 0
	v_pk_fma_f32 v[12:13], v[10:11], v[12:13], v[92:93]
	s_nop 0
	v_pk_fma_f32 v[94:95], v[4:5], v[12:13], v[94:95] op_sel:[0,1,0] op_sel_hi:[1,0,1]
	s_nop 0
	v_pk_fma_f32 v[12:13], v[10:11], v[12:13], v[94:95]
	s_nop 0
	v_pk_fma_f32 v[96:97], v[4:5], v[12:13], v[96:97] op_sel:[0,1,0] op_sel_hi:[1,0,1]
	s_nop 0
	v_pk_fma_f32 v[12:13], v[10:11], v[12:13], v[96:97]
	s_nop 0
	v_pk_fma_f32 v[18:19], v[4:5], v[12:13], v[18:19] op_sel:[0,1,0] op_sel_hi:[1,0,1]
	s_nop 0
	v_pk_fma_f32 v[12:13], v[10:11], v[12:13], v[18:19]
	s_nop 0
	v_pk_fma_f32 v[20:21], v[4:5], v[12:13], v[20:21] op_sel:[0,1,0] op_sel_hi:[1,0,1]
	s_nop 0
	v_pk_fma_f32 v[12:13], v[10:11], v[12:13], v[20:21]
	s_nop 0
	v_pk_fma_f32 v[22:23], v[4:5], v[12:13], v[22:23] op_sel:[0,1,0] op_sel_hi:[1,0,1]
	s_nop 0
	v_pk_fma_f32 v[12:13], v[10:11], v[12:13], v[22:23]
	s_nop 0
	v_pk_fma_f32 v[24:25], v[4:5], v[12:13], v[24:25] op_sel:[0,1,0] op_sel_hi:[1,0,1]
	s_nop 0
	v_pk_fma_f32 v[12:13], v[10:11], v[12:13], v[24:25]
	s_nop 0
	v_mul_lo_u32 v4, v49, s67
	v_lshlrev_b32_e32 v5, 3, v14
	v_readlane_b32 s4, v230, 8
	s_nop 1
	v_add3_u32 v4, s4, v4, v5
	ds_write_b64 v4, v[12:13]
	v_mov_b32_e32 v4, v2

.LBB1_206:
	s_or_b64 exec, exec, s[2:3]
	v_readlane_b32 s2, v230, 10
	v_xor_b32_e32 v2, 0x80000000, v3
	v_mov_b32_e32 v5, v4
	s_waitcnt vmcnt(0)
	v_add3_u32 v6, v45, v48, s2
	s_add_i32 s2, 0, 0xc00
	v_add3_u32 v7, v45, v47, s2
	s_add_i32 s2, 0, 0x600
	v_add3_u32 v10, v45, v46, s2
	s_mov_b32 s2, 0
	v_mov_b32_e32 v26, v44
	v_mov_b32_e32 v34, v44
	v_add_u32_e32 v27, 0x200, v44
	v_add_u32_e32 v35, 0x200, v44
	v_mov_b32_e32 v28, v10
	v_mov_b32_e32 v36, v10
	v_add_u32_e32 v29, 0x200, v10
	v_add_u32_e32 v37, 0x200, v10
	v_mov_b32_e32 v30, v7
	v_mov_b32_e32 v38, v7
	v_add_u32_e32 v31, 0x200, v7
	v_add_u32_e32 v39, 0x200, v7
	v_mov_b32_e32 v32, v6
	v_mov_b32_e32 v40, v6
	v_add_u32_e32 v33, 0x200, v6
	v_add_u32_e32 v41, 0x200, v6
	ds_read2_b32 v[50:51], v26 offset1:96
	ds_read2_b32 v[52:53], v27 offset0:64 offset1:160
	ds_read2_b32 v[54:55], v28 offset1:96
	ds_read2_b32 v[56:57], v29 offset0:64 offset1:160
	v_add_u32_e32 v26, 0x1800, v26
	v_add_u32_e32 v27, 0x1800, v27
	v_add_u32_e32 v28, 0x1800, v28
	v_add_u32_e32 v29, 0x1800, v29
	ds_read2_b32 v[58:59], v30 offset1:96
	ds_read2_b32 v[60:61], v31 offset0:64 offset1:160
	ds_read2_b32 v[62:63], v32 offset1:96
	ds_read2_b32 v[64:65], v33 offset0:64 offset1:160
	v_add_u32_e32 v30, 0x1800, v30
	v_add_u32_e32 v31, 0x1800, v31
	v_add_u32_e32 v32, 0x1800, v32
	v_add_u32_e32 v33, 0x1800, v33
	s_waitcnt lgkmcnt(4)
	v_cvt_f32_f16_e32 v74, v50
	v_cvt_f32_f16_sdwa v75, v50 dst_sel:DWORD dst_unused:UNUSED_PAD src0_sel:WORD_1
	v_cvt_f32_f16_e32 v76, v51
	v_cvt_f32_f16_sdwa v77, v51 dst_sel:DWORD dst_unused:UNUSED_PAD src0_sel:WORD_1
	v_cvt_f32_f16_e32 v78, v52
	v_cvt_f32_f16_sdwa v79, v52 dst_sel:DWORD dst_unused:UNUSED_PAD src0_sel:WORD_1
	v_cvt_f32_f16_e32 v80, v53
	v_cvt_f32_f16_sdwa v81, v53 dst_sel:DWORD dst_unused:UNUSED_PAD src0_sel:WORD_1
	v_cvt_f32_f16_e32 v82, v54
	v_cvt_f32_f16_sdwa v83, v54 dst_sel:DWORD dst_unused:UNUSED_PAD src0_sel:WORD_1
	v_cvt_f32_f16_e32 v84, v55
	v_cvt_f32_f16_sdwa v85, v55 dst_sel:DWORD dst_unused:UNUSED_PAD src0_sel:WORD_1
	v_cvt_f32_f16_e32 v86, v56
	v_cvt_f32_f16_sdwa v87, v56 dst_sel:DWORD dst_unused:UNUSED_PAD src0_sel:WORD_1
	v_cvt_f32_f16_e32 v88, v57
	v_cvt_f32_f16_sdwa v89, v57 dst_sel:DWORD dst_unused:UNUSED_PAD src0_sel:WORD_1
	s_waitcnt lgkmcnt(0)
	ds_read2_b32 v[66:67], v26 offset1:96
	ds_read2_b32 v[68:69], v27 offset0:64 offset1:160
	ds_read2_b32 v[70:71], v28 offset1:96
	ds_read2_b32 v[72:73], v29 offset0:64 offset1:160
	v_add_u32_e32 v26, 0x1800, v26
	v_add_u32_e32 v27, 0x1800, v27
	v_add_u32_e32 v28, 0x1800, v28
	v_add_u32_e32 v29, 0x1800, v29
	v_pk_fma_f32 v[74:75], v[2:3], v[8:9], v[74:75] op_sel:[0,1,0] op_sel_hi:[1,0,1]
	v_cvt_f32_f16_e32 v90, v58
	v_pk_fma_f32 v[8:9], v[4:5], v[8:9], v[74:75]
	v_cvt_f32_f16_sdwa v91, v58 dst_sel:DWORD dst_unused:UNUSED_PAD src0_sel:WORD_1
	v_pk_fma_f32 v[76:77], v[2:3], v[8:9], v[76:77] op_sel:[0,1,0] op_sel_hi:[1,0,1]
	v_cvt_pk_f16_f32 v42, v8, v9
	v_pk_fma_f32 v[8:9], v[4:5], v[8:9], v[76:77]
	v_cvt_f32_f16_e32 v92, v59
	v_cvt_pk_f16_f32 v43, v8, v9
	ds_write2_b32 v34, v42, v43 offset1:96
	v_add_u32_e32 v34, 0x1800, v34
	v_pk_fma_f32 v[78:79], v[2:3], v[8:9], v[78:79] op_sel:[0,1,0] op_sel_hi:[1,0,1]
	v_cvt_f32_f16_sdwa v93, v59 dst_sel:DWORD dst_unused:UNUSED_PAD src0_sel:WORD_1
	v_pk_fma_f32 v[8:9], v[4:5], v[8:9], v[78:79]
	v_cvt_f32_f16_e32 v94, v60
	v_pk_fma_f32 v[80:81], v[2:3], v[8:9], v[80:81] op_sel:[0,1,0] op_sel_hi:[1,0,1]
	v_cvt_pk_f16_f32 v42, v8, v9
	v_pk_fma_f32 v[8:9], v[4:5], v[8:9], v[80:81]
	v_cvt_f32_f16_sdwa v95, v60 dst_sel:DWORD dst_unused:UNUSED_PAD src0_sel:WORD_1
	v_cvt_pk_f16_f32 v43, v8, v9
	ds_write2_b32 v35, v42, v43 offset0:64 offset1:160
	v_add_u32_e32 v35, 0x1800, v35
	v_pk_fma_f32 v[82:83], v[2:3], v[8:9], v[82:83] op_sel:[0,1,0] op_sel_hi:[1,0,1]
	v_cvt_f32_f16_e32 v96, v61
	v_pk_fma_f32 v[8:9], v[4:5], v[8:9], v[82:83]
	v_cvt_f32_f16_sdwa v97, v61 dst_sel:DWORD dst_unused:UNUSED_PAD src0_sel:WORD_1
	v_pk_fma_f32 v[84:85], v[2:3], v[8:9], v[84:85] op_sel:[0,1,0] op_sel_hi:[1,0,1]
	v_cvt_pk_f16_f32 v42, v8, v9
	v_pk_fma_f32 v[8:9], v[4:5], v[8:9], v[84:85]
	v_cvt_f32_f16_e32 v18, v62
	v_cvt_pk_f16_f32 v43, v8, v9
	ds_write2_b32 v36, v42, v43 offset1:96
	v_add_u32_e32 v36, 0x1800, v36
	v_pk_fma_f32 v[86:87], v[2:3], v[8:9], v[86:87] op_sel:[0,1,0] op_sel_hi:[1,0,1]
	v_cvt_f32_f16_sdwa v19, v62 dst_sel:DWORD dst_unused:UNUSED_PAD src0_sel:WORD_1
	v_pk_fma_f32 v[8:9], v[4:5], v[8:9], v[86:87]
	v_cvt_f32_f16_e32 v20, v63
	v_pk_fma_f32 v[88:89], v[2:3], v[8:9], v[88:89] op_sel:[0,1,0] op_sel_hi:[1,0,1]
	v_cvt_pk_f16_f32 v42, v8, v9
	v_pk_fma_f32 v[8:9], v[4:5], v[8:9], v[88:89]
	v_cvt_f32_f16_sdwa v21, v63 dst_sel:DWORD dst_unused:UNUSED_PAD src0_sel:WORD_1
	v_cvt_pk_f16_f32 v43, v8, v9
	ds_write2_b32 v37, v42, v43 offset0:64 offset1:160
	v_add_u32_e32 v37, 0x1800, v37
	v_cvt_f32_f16_e32 v22, v64
	v_cvt_f32_f16_sdwa v23, v64 dst_sel:DWORD dst_unused:UNUSED_PAD src0_sel:WORD_1
	v_cvt_f32_f16_e32 v24, v65
	v_cvt_f32_f16_sdwa v25, v65 dst_sel:DWORD dst_unused:UNUSED_PAD src0_sel:WORD_1
	s_waitcnt lgkmcnt(4)
	ds_read2_b32 v[50:51], v30 offset1:96
	ds_read2_b32 v[52:53], v31 offset0:64 offset1:160
	ds_read2_b32 v[54:55], v32 offset1:96
	ds_read2_b32 v[56:57], v33 offset0:64 offset1:160
	v_add_u32_e32 v30, 0x1800, v30
	v_add_u32_e32 v31, 0x1800, v31
	v_add_u32_e32 v32, 0x1800, v32
	v_add_u32_e32 v33, 0x1800, v33
	v_pk_fma_f32 v[90:91], v[2:3], v[8:9], v[90:91] op_sel:[0,1,0] op_sel_hi:[1,0,1]
	v_cvt_f32_f16_e32 v74, v66
	v_pk_fma_f32 v[8:9], v[4:5], v[8:9], v[90:91]
	v_cvt_f32_f16_sdwa v75, v66 dst_sel:DWORD dst_unused:UNUSED_PAD src0_sel:WORD_1
	v_pk_fma_f32 v[92:93], v[2:3], v[8:9], v[92:93] op_sel:[0,1,0] op_sel_hi:[1,0,1]
	v_cvt_pk_f16_f32 v42, v8, v9
	v_pk_fma_f32 v[8:9], v[4:5], v[8:9], v[92:93]
	v_cvt_f32_f16_e32 v76, v67
	v_cvt_pk_f16_f32 v43, v8, v9
	ds_write2_b32 v38, v42, v43 offset1:96
	v_add_u32_e32 v38, 0x1800, v38
	v_pk_fma_f32 v[94:95], v[2:3], v[8:9], v[94:95] op_sel:[0,1,0] op_sel_hi:[1,0,1]
	v_cvt_f32_f16_sdwa v77, v67 dst_sel:DWORD dst_unused:UNUSED_PAD src0_sel:WORD_1
	v_pk_fma_f32 v[8:9], v[4:5], v[8:9], v[94:95]
	v_cvt_f32_f16_e32 v78, v68
	v_pk_fma_f32 v[96:97], v[2:3], v[8:9], v[96:97] op_sel:[0,1,0] op_sel_hi:[1,0,1]
	v_cvt_pk_f16_f32 v42, v8, v9
	v_pk_fma_f32 v[8:9], v[4:5], v[8:9], v[96:97]
	v_cvt_f32_f16_sdwa v79, v68 dst_sel:DWORD dst_unused:UNUSED_PAD src0_sel:WORD_1
	v_cvt_pk_f16_f32 v43, v8, v9
	ds_write2_b32 v39, v42, v43 offset0:64 offset1:160
	v_add_u32_e32 v39, 0x1800, v39
	v_pk_fma_f32 v[18:19], v[2:3], v[8:9], v[18:19] op_sel:[0,1,0] op_sel_hi:[1,0,1]
	v_cvt_f32_f16_e32 v80, v69
	v_pk_fma_f32 v[8:9], v[4:5], v[8:9], v[18:19]
	v_cvt_f32_f16_sdwa v81, v69 dst_sel:DWORD dst_unused:UNUSED_PAD src0_sel:WORD_1
	v_pk_fma_f32 v[20:21], v[2:3], v[8:9], v[20:21] op_sel:[0,1,0] op_sel_hi:[1,0,1]
	v_cvt_pk_f16_f32 v42, v8, v9
	v_pk_fma_f32 v[8:9], v[4:5], v[8:9], v[20:21]
	v_cvt_f32_f16_e32 v82, v70
	v_cvt_pk_f16_f32 v43, v8, v9
	ds_write2_b32 v40, v42, v43 offset1:96
	v_add_u32_e32 v40, 0x1800, v40
	v_pk_fma_f32 v[22:23], v[2:3], v[8:9], v[22:23] op_sel:[0,1,0] op_sel_hi:[1,0,1]
	v_cvt_f32_f16_sdwa v83, v70 dst_sel:DWORD dst_unused:UNUSED_PAD src0_sel:WORD_1
	v_pk_fma_f32 v[8:9], v[4:5], v[8:9], v[22:23]
	v_cvt_f32_f16_e32 v84, v71
	v_pk_fma_f32 v[24:25], v[2:3], v[8:9], v[24:25] op_sel:[0,1,0] op_sel_hi:[1,0,1]
	v_cvt_pk_f16_f32 v42, v8, v9
	v_pk_fma_f32 v[8:9], v[4:5], v[8:9], v[24:25]
	v_cvt_f32_f16_sdwa v85, v71 dst_sel:DWORD dst_unused:UNUSED_PAD src0_sel:WORD_1
	v_cvt_pk_f16_f32 v43, v8, v9
	ds_write2_b32 v41, v42, v43 offset0:64 offset1:160
	v_add_u32_e32 v41, 0x1800, v41
	v_cvt_f32_f16_e32 v86, v72
	v_cvt_f32_f16_sdwa v87, v72 dst_sel:DWORD dst_unused:UNUSED_PAD src0_sel:WORD_1
	v_cvt_f32_f16_e32 v88, v73
	v_cvt_f32_f16_sdwa v89, v73 dst_sel:DWORD dst_unused:UNUSED_PAD src0_sel:WORD_1
	s_waitcnt lgkmcnt(4)
	ds_read2_b32 v[58:59], v26 offset1:96
	ds_read2_b32 v[60:61], v27 offset0:64 offset1:160
	ds_read2_b32 v[62:63], v28 offset1:96
	ds_read2_b32 v[64:65], v29 offset0:64 offset1:160
	v_add_u32_e32 v26, 0x1800, v26
	v_add_u32_e32 v27, 0x1800, v27
	v_add_u32_e32 v28, 0x1800, v28
	v_add_u32_e32 v29, 0x1800, v29
	v_pk_fma_f32 v[74:75], v[2:3], v[8:9], v[74:75] op_sel:[0,1,0] op_sel_hi:[1,0,1]
	v_cvt_f32_f16_e32 v90, v50
	v_pk_fma_f32 v[8:9], v[4:5], v[8:9], v[74:75]
	v_cvt_f32_f16_sdwa v91, v50 dst_sel:DWORD dst_unused:UNUSED_PAD src0_sel:WORD_1
	v_pk_fma_f32 v[76:77], v[2:3], v[8:9], v[76:77] op_sel:[0,1,0] op_sel_hi:[1,0,1]
	v_cvt_pk_f16_f32 v42, v8, v9
	v_pk_fma_f32 v[8:9], v[4:5], v[8:9], v[76:77]
	v_cvt_f32_f16_e32 v92, v51
	v_cvt_pk_f16_f32 v43, v8, v9
	ds_write2_b32 v34, v42, v43 offset1:96
	v_add_u32_e32 v34, 0x1800, v34
	v_pk_fma_f32 v[78:79], v[2:3], v[8:9], v[78:79] op_sel:[0,1,0] op_sel_hi:[1,0,1]
	v_cvt_f32_f16_sdwa v93, v51 dst_sel:DWORD dst_unused:UNUSED_PAD src0_sel:WORD_1
	v_pk_fma_f32 v[8:9], v[4:5], v[8:9], v[78:79]
	v_cvt_f32_f16_e32 v94, v52
	v_pk_fma_f32 v[80:81], v[2:3], v[8:9], v[80:81] op_sel:[0,1,0] op_sel_hi:[1,0,1]
	v_cvt_pk_f16_f32 v42, v8, v9
	v_pk_fma_f32 v[8:9], v[4:5], v[8:9], v[80:81]
	v_cvt_f32_f16_sdwa v95, v52 dst_sel:DWORD dst_unused:UNUSED_PAD src0_sel:WORD_1
	v_cvt_pk_f16_f32 v43, v8, v9
	ds_write2_b32 v35, v42, v43 offset0:64 offset1:160
	v_add_u32_e32 v35, 0x1800, v35
	v_pk_fma_f32 v[82:83], v[2:3], v[8:9], v[82:83] op_sel:[0,1,0] op_sel_hi:[1,0,1]
	v_cvt_f32_f16_e32 v96, v53
	v_pk_fma_f32 v[8:9], v[4:5], v[8:9], v[82:83]
	v_cvt_f32_f16_sdwa v97, v53 dst_sel:DWORD dst_unused:UNUSED_PAD src0_sel:WORD_1
	v_pk_fma_f32 v[84:85], v[2:3], v[8:9], v[84:85] op_sel:[0,1,0] op_sel_hi:[1,0,1]
	v_cvt_pk_f16_f32 v42, v8, v9
	v_pk_fma_f32 v[8:9], v[4:5], v[8:9], v[84:85]
	v_cvt_f32_f16_e32 v18, v54
	v_cvt_pk_f16_f32 v43, v8, v9
	ds_write2_b32 v36, v42, v43 offset1:96
	v_add_u32_e32 v36, 0x1800, v36
	v_pk_fma_f32 v[86:87], v[2:3], v[8:9], v[86:87] op_sel:[0,1,0] op_sel_hi:[1,0,1]
	v_cvt_f32_f16_sdwa v19, v54 dst_sel:DWORD dst_unused:UNUSED_PAD src0_sel:WORD_1
	v_pk_fma_f32 v[8:9], v[4:5], v[8:9], v[86:87]
	v_cvt_f32_f16_e32 v20, v55
	v_pk_fma_f32 v[88:89], v[2:3], v[8:9], v[88:89] op_sel:[0,1,0] op_sel_hi:[1,0,1]
	v_cvt_pk_f16_f32 v42, v8, v9
	v_pk_fma_f32 v[8:9], v[4:5], v[8:9], v[88:89]
	v_cvt_f32_f16_sdwa v21, v55 dst_sel:DWORD dst_unused:UNUSED_PAD src0_sel:WORD_1
	v_cvt_pk_f16_f32 v43, v8, v9
	ds_write2_b32 v37, v42, v43 offset0:64 offset1:160
	v_add_u32_e32 v37, 0x1800, v37
	v_cvt_f32_f16_e32 v22, v56
	v_cvt_f32_f16_sdwa v23, v56 dst_sel:DWORD dst_unused:UNUSED_PAD src0_sel:WORD_1
	v_cvt_f32_f16_e32 v24, v57
	v_cvt_f32_f16_sdwa v25, v57 dst_sel:DWORD dst_unused:UNUSED_PAD src0_sel:WORD_1
	s_waitcnt lgkmcnt(4)
	ds_read2_b32 v[66:67], v30 offset1:96
	ds_read2_b32 v[68:69], v31 offset0:64 offset1:160
	ds_read2_b32 v[70:71], v32 offset1:96
	ds_read2_b32 v[72:73], v33 offset0:64 offset1:160
	v_add_u32_e32 v30, 0x1800, v30
	v_add_u32_e32 v31, 0x1800, v31
	v_add_u32_e32 v32, 0x1800, v32
	v_add_u32_e32 v33, 0x1800, v33
	v_pk_fma_f32 v[90:91], v[2:3], v[8:9], v[90:91] op_sel:[0,1,0] op_sel_hi:[1,0,1]
	v_cvt_f32_f16_e32 v74, v58
	v_pk_fma_f32 v[8:9], v[4:5], v[8:9], v[90:91]
	v_cvt_f32_f16_sdwa v75, v58 dst_sel:DWORD dst_unused:UNUSED_PAD src0_sel:WORD_1
	v_pk_fma_f32 v[92:93], v[2:3], v[8:9], v[92:93] op_sel:[0,1,0] op_sel_hi:[1,0,1]
	v_cvt_pk_f16_f32 v42, v8, v9
	v_pk_fma_f32 v[8:9], v[4:5], v[8:9], v[92:93]
	v_cvt_f32_f16_e32 v76, v59
	v_cvt_pk_f16_f32 v43, v8, v9
	ds_write2_b32 v38, v42, v43 offset1:96
	v_add_u32_e32 v38, 0x1800, v38
	v_pk_fma_f32 v[94:95], v[2:3], v[8:9], v[94:95] op_sel:[0,1,0] op_sel_hi:[1,0,1]
	v_cvt_f32_f16_sdwa v77, v59 dst_sel:DWORD dst_unused:UNUSED_PAD src0_sel:WORD_1
	v_pk_fma_f32 v[8:9], v[4:5], v[8:9], v[94:95]
	v_cvt_f32_f16_e32 v78, v60
	v_pk_fma_f32 v[96:97], v[2:3], v[8:9], v[96:97] op_sel:[0,1,0] op_sel_hi:[1,0,1]
	v_cvt_pk_f16_f32 v42, v8, v9
	v_pk_fma_f32 v[8:9], v[4:5], v[8:9], v[96:97]
	v_cvt_f32_f16_sdwa v79, v60 dst_sel:DWORD dst_unused:UNUSED_PAD src0_sel:WORD_1
	v_cvt_pk_f16_f32 v43, v8, v9
	ds_write2_b32 v39, v42, v43 offset0:64 offset1:160
	v_add_u32_e32 v39, 0x1800, v39
	v_pk_fma_f32 v[18:19], v[2:3], v[8:9], v[18:19] op_sel:[0,1,0] op_sel_hi:[1,0,1]
	v_cvt_f32_f16_e32 v80, v61
	v_pk_fma_f32 v[8:9], v[4:5], v[8:9], v[18:19]
	v_cvt_f32_f16_sdwa v81, v61 dst_sel:DWORD dst_unused:UNUSED_PAD src0_sel:WORD_1
	v_pk_fma_f32 v[20:21], v[2:3], v[8:9], v[20:21] op_sel:[0,1,0] op_sel_hi:[1,0,1]
	v_cvt_pk_f16_f32 v42, v8, v9
	v_pk_fma_f32 v[8:9], v[4:5], v[8:9], v[20:21]
	v_cvt_f32_f16_e32 v82, v62
	v_cvt_pk_f16_f32 v43, v8, v9
	ds_write2_b32 v40, v42, v43 offset1:96
	v_add_u32_e32 v40, 0x1800, v40
	v_pk_fma_f32 v[22:23], v[2:3], v[8:9], v[22:23] op_sel:[0,1,0] op_sel_hi:[1,0,1]
	v_cvt_f32_f16_sdwa v83, v62 dst_sel:DWORD dst_unused:UNUSED_PAD src0_sel:WORD_1
	v_pk_fma_f32 v[8:9], v[4:5], v[8:9], v[22:23]
	v_cvt_f32_f16_e32 v84, v63
	v_pk_fma_f32 v[24:25], v[2:3], v[8:9], v[24:25] op_sel:[0,1,0] op_sel_hi:[1,0,1]
	v_cvt_pk_f16_f32 v42, v8, v9
	v_pk_fma_f32 v[8:9], v[4:5], v[8:9], v[24:25]
	v_cvt_f32_f16_sdwa v85, v63 dst_sel:DWORD dst_unused:UNUSED_PAD src0_sel:WORD_1
	v_cvt_pk_f16_f32 v43, v8, v9
	ds_write2_b32 v41, v42, v43 offset0:64 offset1:160
	v_add_u32_e32 v41, 0x1800, v41
	v_cvt_f32_f16_e32 v86, v64
	v_cvt_f32_f16_sdwa v87, v64 dst_sel:DWORD dst_unused:UNUSED_PAD src0_sel:WORD_1
	v_cvt_f32_f16_e32 v88, v65
	v_cvt_f32_f16_sdwa v89, v65 dst_sel:DWORD dst_unused:UNUSED_PAD src0_sel:WORD_1
	s_waitcnt lgkmcnt(4)
	ds_read2_b32 v[50:51], v26 offset1:96
	ds_read2_b32 v[52:53], v27 offset0:64 offset1:160
	ds_read2_b32 v[54:55], v28 offset1:96
	ds_read2_b32 v[56:57], v29 offset0:64 offset1:160
	v_add_u32_e32 v26, 0x1800, v26
	v_add_u32_e32 v27, 0x1800, v27
	v_add_u32_e32 v28, 0x1800, v28
	v_add_u32_e32 v29, 0x1800, v29
	v_pk_fma_f32 v[74:75], v[2:3], v[8:9], v[74:75] op_sel:[0,1,0] op_sel_hi:[1,0,1]
	v_cvt_f32_f16_e32 v90, v66
	v_pk_fma_f32 v[8:9], v[4:5], v[8:9], v[74:75]
	v_cvt_f32_f16_sdwa v91, v66 dst_sel:DWORD dst_unused:UNUSED_PAD src0_sel:WORD_1
	v_pk_fma_f32 v[76:77], v[2:3], v[8:9], v[76:77] op_sel:[0,1,0] op_sel_hi:[1,0,1]
	v_cvt_pk_f16_f32 v42, v8, v9
	v_pk_fma_f32 v[8:9], v[4:5], v[8:9], v[76:77]
	v_cvt_f32_f16_e32 v92, v67
	v_cvt_pk_f16_f32 v43, v8, v9
	ds_write2_b32 v34, v42, v43 offset1:96
	v_add_u32_e32 v34, 0x1800, v34
	v_pk_fma_f32 v[78:79], v[2:3], v[8:9], v[78:79] op_sel:[0,1,0] op_sel_hi:[1,0,1]
	v_cvt_f32_f16_sdwa v93, v67 dst_sel:DWORD dst_unused:UNUSED_PAD src0_sel:WORD_1
	v_pk_fma_f32 v[8:9], v[4:5], v[8:9], v[78:79]
	v_cvt_f32_f16_e32 v94, v68
	v_pk_fma_f32 v[80:81], v[2:3], v[8:9], v[80:81] op_sel:[0,1,0] op_sel_hi:[1,0,1]
	v_cvt_pk_f16_f32 v42, v8, v9
	v_pk_fma_f32 v[8:9], v[4:5], v[8:9], v[80:81]
	v_cvt_f32_f16_sdwa v95, v68 dst_sel:DWORD dst_unused:UNUSED_PAD src0_sel:WORD_1
	v_cvt_pk_f16_f32 v43, v8, v9
	ds_write2_b32 v35, v42, v43 offset0:64 offset1:160
	v_add_u32_e32 v35, 0x1800, v35
	v_pk_fma_f32 v[82:83], v[2:3], v[8:9], v[82:83] op_sel:[0,1,0] op_sel_hi:[1,0,1]
	v_cvt_f32_f16_e32 v96, v69
	v_pk_fma_f32 v[8:9], v[4:5], v[8:9], v[82:83]
	v_cvt_f32_f16_sdwa v97, v69 dst_sel:DWORD dst_unused:UNUSED_PAD src0_sel:WORD_1
	v_pk_fma_f32 v[84:85], v[2:3], v[8:9], v[84:85] op_sel:[0,1,0] op_sel_hi:[1,0,1]
	v_cvt_pk_f16_f32 v42, v8, v9
	v_pk_fma_f32 v[8:9], v[4:5], v[8:9], v[84:85]
	v_cvt_f32_f16_e32 v18, v70
	v_cvt_pk_f16_f32 v43, v8, v9
	ds_write2_b32 v36, v42, v43 offset1:96
	v_add_u32_e32 v36, 0x1800, v36
	v_pk_fma_f32 v[86:87], v[2:3], v[8:9], v[86:87] op_sel:[0,1,0] op_sel_hi:[1,0,1]
	v_cvt_f32_f16_sdwa v19, v70 dst_sel:DWORD dst_unused:UNUSED_PAD src0_sel:WORD_1
	v_pk_fma_f32 v[8:9], v[4:5], v[8:9], v[86:87]
	v_cvt_f32_f16_e32 v20, v71
	v_pk_fma_f32 v[88:89], v[2:3], v[8:9], v[88:89] op_sel:[0,1,0] op_sel_hi:[1,0,1]
	v_cvt_pk_f16_f32 v42, v8, v9
	v_pk_fma_f32 v[8:9], v[4:5], v[8:9], v[88:89]
	v_cvt_f32_f16_sdwa v21, v71 dst_sel:DWORD dst_unused:UNUSED_PAD src0_sel:WORD_1
	v_cvt_pk_f16_f32 v43, v8, v9
	ds_write2_b32 v37, v42, v43 offset0:64 offset1:160
	v_add_u32_e32 v37, 0x1800, v37
	v_cvt_f32_f16_e32 v22, v72
	v_cvt_f32_f16_sdwa v23, v72 dst_sel:DWORD dst_unused:UNUSED_PAD src0_sel:WORD_1
	v_cvt_f32_f16_e32 v24, v73
	v_cvt_f32_f16_sdwa v25, v73 dst_sel:DWORD dst_unused:UNUSED_PAD src0_sel:WORD_1
	s_waitcnt lgkmcnt(4)
	ds_read2_b32 v[58:59], v30 offset1:96
	ds_read2_b32 v[60:61], v31 offset0:64 offset1:160
	ds_read2_b32 v[62:63], v32 offset1:96
	ds_read2_b32 v[64:65], v33 offset0:64 offset1:160
	v_add_u32_e32 v30, 0x1800, v30
	v_add_u32_e32 v31, 0x1800, v31
	v_add_u32_e32 v32, 0x1800, v32
	v_add_u32_e32 v33, 0x1800, v33
	v_pk_fma_f32 v[90:91], v[2:3], v[8:9], v[90:91] op_sel:[0,1,0] op_sel_hi:[1,0,1]
	v_cvt_f32_f16_e32 v74, v50
	v_pk_fma_f32 v[8:9], v[4:5], v[8:9], v[90:91]
	v_cvt_f32_f16_sdwa v75, v50 dst_sel:DWORD dst_unused:UNUSED_PAD src0_sel:WORD_1
	v_pk_fma_f32 v[92:93], v[2:3], v[8:9], v[92:93] op_sel:[0,1,0] op_sel_hi:[1,0,1]
	v_cvt_pk_f16_f32 v42, v8, v9
	v_pk_fma_f32 v[8:9], v[4:5], v[8:9], v[92:93]
	v_cvt_f32_f16_e32 v76, v51
	v_cvt_pk_f16_f32 v43, v8, v9
	ds_write2_b32 v38, v42, v43 offset1:96
	v_add_u32_e32 v38, 0x1800, v38
	v_pk_fma_f32 v[94:95], v[2:3], v[8:9], v[94:95] op_sel:[0,1,0] op_sel_hi:[1,0,1]
	v_cvt_f32_f16_sdwa v77, v51 dst_sel:DWORD dst_unused:UNUSED_PAD src0_sel:WORD_1
	v_pk_fma_f32 v[8:9], v[4:5], v[8:9], v[94:95]
	v_cvt_f32_f16_e32 v78, v52
	v_pk_fma_f32 v[96:97], v[2:3], v[8:9], v[96:97] op_sel:[0,1,0] op_sel_hi:[1,0,1]
	v_cvt_pk_f16_f32 v42, v8, v9
	v_pk_fma_f32 v[8:9], v[4:5], v[8:9], v[96:97]
	v_cvt_f32_f16_sdwa v79, v52 dst_sel:DWORD dst_unused:UNUSED_PAD src0_sel:WORD_1
	v_cvt_pk_f16_f32 v43, v8, v9
	ds_write2_b32 v39, v42, v43 offset0:64 offset1:160
	v_add_u32_e32 v39, 0x1800, v39
	v_pk_fma_f32 v[18:19], v[2:3], v[8:9], v[18:19] op_sel:[0,1,0] op_sel_hi:[1,0,1]
	v_cvt_f32_f16_e32 v80, v53
	v_pk_fma_f32 v[8:9], v[4:5], v[8:9], v[18:19]
	v_cvt_f32_f16_sdwa v81, v53 dst_sel:DWORD dst_unused:UNUSED_PAD src0_sel:WORD_1
	v_pk_fma_f32 v[20:21], v[2:3], v[8:9], v[20:21] op_sel:[0,1,0] op_sel_hi:[1,0,1]
	v_cvt_pk_f16_f32 v42, v8, v9
	v_pk_fma_f32 v[8:9], v[4:5], v[8:9], v[20:21]
	v_cvt_f32_f16_e32 v82, v54
	v_cvt_pk_f16_f32 v43, v8, v9
	ds_write2_b32 v40, v42, v43 offset1:96
	v_add_u32_e32 v40, 0x1800, v40
	v_pk_fma_f32 v[22:23], v[2:3], v[8:9], v[22:23] op_sel:[0,1,0] op_sel_hi:[1,0,1]
	v_cvt_f32_f16_sdwa v83, v54 dst_sel:DWORD dst_unused:UNUSED_PAD src0_sel:WORD_1
	v_pk_fma_f32 v[8:9], v[4:5], v[8:9], v[22:23]
	v_cvt_f32_f16_e32 v84, v55
	v_pk_fma_f32 v[24:25], v[2:3], v[8:9], v[24:25] op_sel:[0,1,0] op_sel_hi:[1,0,1]
	v_cvt_pk_f16_f32 v42, v8, v9
	v_pk_fma_f32 v[8:9], v[4:5], v[8:9], v[24:25]
	v_cvt_f32_f16_sdwa v85, v55 dst_sel:DWORD dst_unused:UNUSED_PAD src0_sel:WORD_1
	v_cvt_pk_f16_f32 v43, v8, v9
	ds_write2_b32 v41, v42, v43 offset0:64 offset1:160
	v_add_u32_e32 v41, 0x1800, v41
	v_cvt_f32_f16_e32 v86, v56
	v_cvt_f32_f16_sdwa v87, v56 dst_sel:DWORD dst_unused:UNUSED_PAD src0_sel:WORD_1
	v_cvt_f32_f16_e32 v88, v57
	v_cvt_f32_f16_sdwa v89, v57 dst_sel:DWORD dst_unused:UNUSED_PAD src0_sel:WORD_1
	s_waitcnt lgkmcnt(4)
	v_pk_fma_f32 v[74:75], v[2:3], v[8:9], v[74:75] op_sel:[0,1,0] op_sel_hi:[1,0,1]
	v_cvt_f32_f16_e32 v90, v58
	v_pk_fma_f32 v[8:9], v[4:5], v[8:9], v[74:75]
	v_cvt_f32_f16_sdwa v91, v58 dst_sel:DWORD dst_unused:UNUSED_PAD src0_sel:WORD_1
	v_pk_fma_f32 v[76:77], v[2:3], v[8:9], v[76:77] op_sel:[0,1,0] op_sel_hi:[1,0,1]
	v_cvt_pk_f16_f32 v42, v8, v9
	v_pk_fma_f32 v[8:9], v[4:5], v[8:9], v[76:77]
	v_cvt_f32_f16_e32 v92, v59
	v_cvt_pk_f16_f32 v43, v8, v9
	ds_write2_b32 v34, v42, v43 offset1:96
	v_add_u32_e32 v34, 0x1800, v34
	v_pk_fma_f32 v[78:79], v[2:3], v[8:9], v[78:79] op_sel:[0,1,0] op_sel_hi:[1,0,1]
	v_cvt_f32_f16_sdwa v93, v59 dst_sel:DWORD dst_unused:UNUSED_PAD src0_sel:WORD_1
	v_pk_fma_f32 v[8:9], v[4:5], v[8:9], v[78:79]
	v_cvt_f32_f16_e32 v94, v60
	v_pk_fma_f32 v[80:81], v[2:3], v[8:9], v[80:81] op_sel:[0,1,0] op_sel_hi:[1,0,1]
	v_cvt_pk_f16_f32 v42, v8, v9
	v_pk_fma_f32 v[8:9], v[4:5], v[8:9], v[80:81]
	v_cvt_f32_f16_sdwa v95, v60 dst_sel:DWORD dst_unused:UNUSED_PAD src0_sel:WORD_1
	v_cvt_pk_f16_f32 v43, v8, v9
	ds_write2_b32 v35, v42, v43 offset0:64 offset1:160
	v_add_u32_e32 v35, 0x1800, v35
	v_pk_fma_f32 v[82:83], v[2:3], v[8:9], v[82:83] op_sel:[0,1,0] op_sel_hi:[1,0,1]
	v_cvt_f32_f16_e32 v96, v61
	v_pk_fma_f32 v[8:9], v[4:5], v[8:9], v[82:83]
	v_cvt_f32_f16_sdwa v97, v61 dst_sel:DWORD dst_unused:UNUSED_PAD src0_sel:WORD_1
	v_pk_fma_f32 v[84:85], v[2:3], v[8:9], v[84:85] op_sel:[0,1,0] op_sel_hi:[1,0,1]
	v_cvt_pk_f16_f32 v42, v8, v9
	v_pk_fma_f32 v[8:9], v[4:5], v[8:9], v[84:85]
	v_cvt_f32_f16_e32 v18, v62
	v_cvt_pk_f16_f32 v43, v8, v9
	ds_write2_b32 v36, v42, v43 offset1:96
	v_add_u32_e32 v36, 0x1800, v36
	v_pk_fma_f32 v[86:87], v[2:3], v[8:9], v[86:87] op_sel:[0,1,0] op_sel_hi:[1,0,1]
	v_cvt_f32_f16_sdwa v19, v62 dst_sel:DWORD dst_unused:UNUSED_PAD src0_sel:WORD_1
	v_pk_fma_f32 v[8:9], v[4:5], v[8:9], v[86:87]
	v_cvt_f32_f16_e32 v20, v63
	v_pk_fma_f32 v[88:89], v[2:3], v[8:9], v[88:89] op_sel:[0,1,0] op_sel_hi:[1,0,1]
	v_cvt_pk_f16_f32 v42, v8, v9
	v_pk_fma_f32 v[8:9], v[4:5], v[8:9], v[88:89]
	v_cvt_f32_f16_sdwa v21, v63 dst_sel:DWORD dst_unused:UNUSED_PAD src0_sel:WORD_1
	v_cvt_pk_f16_f32 v43, v8, v9
	ds_write2_b32 v37, v42, v43 offset0:64 offset1:160
	v_add_u32_e32 v37, 0x1800, v37
	v_cvt_f32_f16_e32 v22, v64
	v_cvt_f32_f16_sdwa v23, v64 dst_sel:DWORD dst_unused:UNUSED_PAD src0_sel:WORD_1
	v_cvt_f32_f16_e32 v24, v65
	v_cvt_f32_f16_sdwa v25, v65 dst_sel:DWORD dst_unused:UNUSED_PAD src0_sel:WORD_1
	v_pk_fma_f32 v[90:91], v[2:3], v[8:9], v[90:91] op_sel:[0,1,0] op_sel_hi:[1,0,1]
	s_nop 0
	v_pk_fma_f32 v[8:9], v[4:5], v[8:9], v[90:91]
	s_nop 0
	v_pk_fma_f32 v[92:93], v[2:3], v[8:9], v[92:93] op_sel:[0,1,0] op_sel_hi:[1,0,1]
	v_cvt_pk_f16_f32 v42, v8, v9
	v_pk_fma_f32 v[8:9], v[4:5], v[8:9], v[92:93]
	s_nop 0
	v_cvt_pk_f16_f32 v43, v8, v9
	ds_write2_b32 v38, v42, v43 offset1:96
	v_add_u32_e32 v38, 0x1800, v38
	v_pk_fma_f32 v[94:95], v[2:3], v[8:9], v[94:95] op_sel:[0,1,0] op_sel_hi:[1,0,1]
	s_nop 0
	v_pk_fma_f32 v[8:9], v[4:5], v[8:9], v[94:95]
	s_nop 0
	v_pk_fma_f32 v[96:97], v[2:3], v[8:9], v[96:97] op_sel:[0,1,0] op_sel_hi:[1,0,1]
	v_cvt_pk_f16_f32 v42, v8, v9
	v_pk_fma_f32 v[8:9], v[4:5], v[8:9], v[96:97]
	s_nop 0
	v_cvt_pk_f16_f32 v43, v8, v9
	ds_write2_b32 v39, v42, v43 offset0:64 offset1:160
	v_add_u32_e32 v39, 0x1800, v39
	v_pk_fma_f32 v[18:19], v[2:3], v[8:9], v[18:19] op_sel:[0,1,0] op_sel_hi:[1,0,1]
	s_nop 0
	v_pk_fma_f32 v[8:9], v[4:5], v[8:9], v[18:19]
	s_nop 0
	v_pk_fma_f32 v[20:21], v[2:3], v[8:9], v[20:21] op_sel:[0,1,0] op_sel_hi:[1,0,1]
	v_cvt_pk_f16_f32 v42, v8, v9
	v_pk_fma_f32 v[8:9], v[4:5], v[8:9], v[20:21]
	s_nop 0
	v_cvt_pk_f16_f32 v43, v8, v9
	ds_write2_b32 v40, v42, v43 offset1:96
	v_add_u32_e32 v40, 0x1800, v40
	v_pk_fma_f32 v[22:23], v[2:3], v[8:9], v[22:23] op_sel:[0,1,0] op_sel_hi:[1,0,1]
	s_nop 0
	v_pk_fma_f32 v[8:9], v[4:5], v[8:9], v[22:23]
	s_nop 0
	v_pk_fma_f32 v[24:25], v[2:3], v[8:9], v[24:25] op_sel:[0,1,0] op_sel_hi:[1,0,1]
	v_cvt_pk_f16_f32 v42, v8, v9
	v_pk_fma_f32 v[8:9], v[4:5], v[8:9], v[24:25]
	s_nop 0
	v_cvt_pk_f16_f32 v43, v8, v9
	ds_write2_b32 v41, v42, v43 offset0:64 offset1:160
	v_add_u32_e32 v41, 0x1800, v41
